# LSTM tail: 2*qc obtained as rcp(0.5*e+0.5) (bit-exact power-of-two scaling) so the -2*og multiply disappears; og rcp moved into the exp->fma wait slot
# baseline (speedup 1.0000x reference)
.Llstm3_loop:
	ds_read_b128 v[184:187], v209 offset:0
	ds_read_b128 v[188:191], v209 offset:64
	ds_read_b128 v[176:179], v211 offset:0
	ds_read_b128 v[180:183], v211 offset:64
	v_mfma_f32_16x16x32_f16 v[164:167], v[68:71], v[148:151], v[164:167]
	s_waitcnt vmcnt(4)
	v_mfma_f32_16x16x32_f16 v[160:163], v[60:63], v[156:159], v[160:163]
	s_waitcnt lgkmcnt(3)
	v_mfma_f32_16x16x32_f16 v[168:171], v[16:19], v[184:187], v[192:195]
	v_mfma_f32_16x16x32_f16 v[172:175], v[24:27], v[184:187], v[192:195]
	s_waitcnt lgkmcnt(2)
	v_mfma_f32_16x16x32_f16 v[168:171], v[20:23], v[188:191], v[168:171]
	v_mfma_f32_16x16x32_f16 v[172:175], v[28:31], v[188:191], v[172:175]
	s_waitcnt lgkmcnt(1)
	v_mfma_f32_16x16x32_f16 v[168:171], v[32:35], v[176:179], v[168:171]
	v_mfma_f32_16x16x32_f16 v[172:175], v[40:43], v[176:179], v[172:175]
	s_waitcnt lgkmcnt(0)
	v_mfma_f32_16x16x32_f16 v[168:171], v[36:39], v[180:183], v[168:171]
	v_mfma_f32_16x16x32_f16 v[172:175], v[44:47], v[180:183], v[172:175]
	s_nop 7
	v_mov_b32_dpp v168, v172 quad_perm:[0,1,2,3] row_mask:0xf bank_mask:0xa
	v_mov_b32_dpp v169, v173 quad_perm:[0,1,2,3] row_mask:0xf bank_mask:0xa
	v_mov_b32_dpp v170, v174 quad_perm:[0,1,2,3] row_mask:0xf bank_mask:0xa
	v_exp_f32_e32 v200, v168
	v_mov_b32_dpp v171, v175 quad_perm:[0,1,2,3] row_mask:0xf bank_mask:0xa
	v_exp_f32_e32 v201, v169
	v_exp_f32_e32 v202, v170
	v_exp_f32_e32 v203, v171
	v_pk_add_f32 v[200:201], v[200:201], 1.0 op_sel_hi:[1,0]
	v_pk_add_f32 v[202:203], v[202:203], 1.0 op_sel_hi:[1,0]
	v_rcp_f32_e32 v202, v202
	v_rcp_f32_e32 v200, v200
	v_rcp_f32_e32 v201, v201
	v_fmamk_f32 v204, v202, 0xc0b8aa3b, v222
	v_mul_f32_e32 v205, v200, v204
	v_fma_f32 v220, v201, v220, v205
	v_exp_f32_e32 v206, v220
	v_rcp_f32_e32 v203, v203
	v_fma_f32 v206, v206, 0.5, 0.5
	v_rcp_f32_e32 v206, v206
	v_max_f32_e32 v221, v221, v215
	v_fma_mixlo_f16 v208, -v206, v203, v203
	ds_write_b16 v225, v208 offset:576
	v_fma_f32 v215, -v206, v203, v203
	v_mfma_f32_16x16x32_f16 v[232:235], v[80:83], v[144:147], v[120:123]
	v_mfma_f32_16x16x32_f16 v[164:167], v[72:75], v[152:155], v[164:167]
	ds_write_b128 v227, v[160:163] offset:4352
	ds_read_b128 v[196:199], v226 offset:1088
	s_waitcnt lgkmcnt(2)
	s_barrier
	ds_read_b128 v[184:187], v210 offset:576
	ds_read_b128 v[188:191], v210 offset:640
	ds_read_b128 v[176:179], v212 offset:576
	ds_read_b128 v[180:183], v212 offset:640
	v_mfma_f32_16x16x32_f16 v[232:235], v[84:87], v[148:151], v[232:235]
	v_mfma_f32_16x16x32_f16 v[164:167], v[76:79], v[156:159], v[164:167]
	s_waitcnt lgkmcnt(3)
	v_mfma_f32_16x16x32_f16 v[168:171], v[16:19], v[184:187], v[196:199]
	v_mfma_f32_16x16x32_f16 v[172:175], v[24:27], v[184:187], v[196:199]
	s_waitcnt lgkmcnt(2)
	v_mfma_f32_16x16x32_f16 v[168:171], v[20:23], v[188:191], v[168:171]
	v_mfma_f32_16x16x32_f16 v[172:175], v[28:31], v[188:191], v[172:175]
	s_waitcnt lgkmcnt(1)
	v_mfma_f32_16x16x32_f16 v[168:171], v[32:35], v[176:179], v[168:171]
	v_mfma_f32_16x16x32_f16 v[172:175], v[40:43], v[176:179], v[172:175]
	s_waitcnt lgkmcnt(0)
	v_mfma_f32_16x16x32_f16 v[168:171], v[36:39], v[180:183], v[168:171]
	v_mfma_f32_16x16x32_f16 v[172:175], v[44:47], v[180:183], v[172:175]
	s_nop 7
	v_mov_b32_dpp v168, v172 quad_perm:[0,1,2,3] row_mask:0xf bank_mask:0xa
	v_mov_b32_dpp v169, v173 quad_perm:[0,1,2,3] row_mask:0xf bank_mask:0xa
	v_mov_b32_dpp v170, v174 quad_perm:[0,1,2,3] row_mask:0xf bank_mask:0xa
	v_exp_f32_e32 v200, v168
	v_mov_b32_dpp v171, v175 quad_perm:[0,1,2,3] row_mask:0xf bank_mask:0xa
	v_exp_f32_e32 v201, v169
	v_exp_f32_e32 v202, v170
	v_exp_f32_e32 v203, v171
	v_pk_add_f32 v[200:201], v[200:201], 1.0 op_sel_hi:[1,0]
	v_pk_add_f32 v[202:203], v[202:203], 1.0 op_sel_hi:[1,0]
	v_rcp_f32_e32 v202, v202
	v_rcp_f32_e32 v200, v200
	v_rcp_f32_e32 v201, v201
	v_fmamk_f32 v204, v202, 0xc0b8aa3b, v222
	v_mul_f32_e32 v205, v200, v204
	v_fma_f32 v220, v201, v220, v205
	v_exp_f32_e32 v206, v220
	v_rcp_f32_e32 v203, v203
	v_fma_f32 v206, v206, 0.5, 0.5
	v_rcp_f32_e32 v206, v206
	v_max_f32_e32 v221, v221, v215
	v_fma_mixlo_f16 v208, -v206, v203, v203
	ds_write_b16 v225, v208 offset:0
	v_fma_f32 v215, -v206, v203, v203
	v_mfma_f32_16x16x32_f16 v[236:239], v[96:99], v[144:147], v[124:127]
	v_mfma_f32_16x16x32_f16 v[232:235], v[88:91], v[152:155], v[232:235]
	global_load_dwordx4 v[144:147], v[228:229], off offset:0
	ds_write_b128 v227, v[164:167] offset:4416
	ds_read_b128 v[192:195], v226 offset:2176
	s_waitcnt lgkmcnt(2)
	s_barrier
	ds_read_b128 v[184:187], v209 offset:0
	ds_read_b128 v[188:191], v209 offset:64
	ds_read_b128 v[176:179], v211 offset:0
	ds_read_b128 v[180:183], v211 offset:64
	v_mfma_f32_16x16x32_f16 v[236:239], v[100:103], v[148:151], v[236:239]
	v_mfma_f32_16x16x32_f16 v[232:235], v[92:95], v[156:159], v[232:235]
	global_load_dwordx4 v[148:151], v[228:229], off offset:64
	s_waitcnt lgkmcnt(3)
	v_mfma_f32_16x16x32_f16 v[168:171], v[16:19], v[184:187], v[192:195]
	v_mfma_f32_16x16x32_f16 v[172:175], v[24:27], v[184:187], v[192:195]
	s_waitcnt lgkmcnt(2)
	v_mfma_f32_16x16x32_f16 v[168:171], v[20:23], v[188:191], v[168:171]
	v_mfma_f32_16x16x32_f16 v[172:175], v[28:31], v[188:191], v[172:175]
	s_waitcnt lgkmcnt(1)
	v_mfma_f32_16x16x32_f16 v[168:171], v[32:35], v[176:179], v[168:171]
	v_mfma_f32_16x16x32_f16 v[172:175], v[40:43], v[176:179], v[172:175]
	s_waitcnt lgkmcnt(0)
	v_mfma_f32_16x16x32_f16 v[168:171], v[36:39], v[180:183], v[168:171]
	v_mfma_f32_16x16x32_f16 v[172:175], v[44:47], v[180:183], v[172:175]
	s_nop 7
	v_mov_b32_dpp v168, v172 quad_perm:[0,1,2,3] row_mask:0xf bank_mask:0xa
	v_mov_b32_dpp v169, v173 quad_perm:[0,1,2,3] row_mask:0xf bank_mask:0xa
	v_mov_b32_dpp v170, v174 quad_perm:[0,1,2,3] row_mask:0xf bank_mask:0xa
	v_exp_f32_e32 v200, v168
	v_mov_b32_dpp v171, v175 quad_perm:[0,1,2,3] row_mask:0xf bank_mask:0xa
	v_exp_f32_e32 v201, v169
	v_exp_f32_e32 v202, v170
	v_exp_f32_e32 v203, v171
	v_pk_add_f32 v[200:201], v[200:201], 1.0 op_sel_hi:[1,0]
	v_pk_add_f32 v[202:203], v[202:203], 1.0 op_sel_hi:[1,0]
	v_rcp_f32_e32 v202, v202
	v_rcp_f32_e32 v200, v200
	v_rcp_f32_e32 v201, v201
	v_fmamk_f32 v204, v202, 0xc0b8aa3b, v222
	v_mul_f32_e32 v205, v200, v204
	v_fma_f32 v220, v201, v220, v205
	v_exp_f32_e32 v206, v220
	v_rcp_f32_e32 v203, v203
	v_fma_f32 v206, v206, 0.5, 0.5
	v_rcp_f32_e32 v206, v206
	v_max_f32_e32 v221, v221, v215
	v_fma_mixlo_f16 v208, -v206, v203, v203
	ds_write_b16 v225, v208 offset:576
	v_fma_f32 v215, -v206, v203, v203
	s_waitcnt vmcnt(5)
	v_mfma_f32_16x16x32_f16 v[160:163], v[48:51], v[128:131], v[112:115]
	v_mfma_f32_16x16x32_f16 v[236:239], v[104:107], v[152:155], v[236:239]
	global_load_dwordx4 v[152:155], v[228:229], off offset:128
	ds_write_b128 v227, v[232:235] offset:4480
	ds_read_b128 v[196:199], v226 offset:3264
	s_waitcnt lgkmcnt(2)
	s_barrier
	ds_read_b128 v[184:187], v210 offset:576
	ds_read_b128 v[188:191], v210 offset:640
	ds_read_b128 v[176:179], v212 offset:576
	ds_read_b128 v[180:183], v212 offset:640
	s_waitcnt vmcnt(5)
	v_mfma_f32_16x16x32_f16 v[160:163], v[52:55], v[132:135], v[160:163]
	v_mfma_f32_16x16x32_f16 v[236:239], v[108:111], v[156:159], v[236:239]
	global_load_dwordx4 v[156:159], v[228:229], off offset:192
	v_lshl_add_u64 v[228:229], v[228:229], 0, s[20:21]
	s_waitcnt lgkmcnt(3)
	v_mfma_f32_16x16x32_f16 v[168:171], v[16:19], v[184:187], v[196:199]
	v_mfma_f32_16x16x32_f16 v[172:175], v[24:27], v[184:187], v[196:199]
	s_waitcnt lgkmcnt(2)
	v_mfma_f32_16x16x32_f16 v[168:171], v[20:23], v[188:191], v[168:171]
	v_mfma_f32_16x16x32_f16 v[172:175], v[28:31], v[188:191], v[172:175]
	s_waitcnt lgkmcnt(1)
	v_mfma_f32_16x16x32_f16 v[168:171], v[32:35], v[176:179], v[168:171]
	v_mfma_f32_16x16x32_f16 v[172:175], v[40:43], v[176:179], v[172:175]
	s_waitcnt lgkmcnt(0)
	v_mfma_f32_16x16x32_f16 v[168:171], v[36:39], v[180:183], v[168:171]
	v_mfma_f32_16x16x32_f16 v[172:175], v[44:47], v[180:183], v[172:175]
	s_nop 7
	v_mov_b32_dpp v168, v172 quad_perm:[0,1,2,3] row_mask:0xf bank_mask:0xa
	v_mov_b32_dpp v169, v173 quad_perm:[0,1,2,3] row_mask:0xf bank_mask:0xa
	v_mov_b32_dpp v170, v174 quad_perm:[0,1,2,3] row_mask:0xf bank_mask:0xa
	v_exp_f32_e32 v200, v168
	v_mov_b32_dpp v171, v175 quad_perm:[0,1,2,3] row_mask:0xf bank_mask:0xa
	v_exp_f32_e32 v201, v169
	v_exp_f32_e32 v202, v170
	v_exp_f32_e32 v203, v171
	v_pk_add_f32 v[200:201], v[200:201], 1.0 op_sel_hi:[1,0]
	v_pk_add_f32 v[202:203], v[202:203], 1.0 op_sel_hi:[1,0]
	v_rcp_f32_e32 v202, v202
	v_rcp_f32_e32 v200, v200
	v_rcp_f32_e32 v201, v201
	v_fmamk_f32 v204, v202, 0xc0b8aa3b, v222
	v_mul_f32_e32 v205, v200, v204
	v_fma_f32 v220, v201, v220, v205
	v_exp_f32_e32 v206, v220
	v_rcp_f32_e32 v203, v203
	v_fma_f32 v206, v206, 0.5, 0.5
	v_rcp_f32_e32 v206, v206
	v_max_f32_e32 v221, v221, v215
	v_fma_mixlo_f16 v208, -v206, v203, v203
	ds_write_b16 v225, v208 offset:0
	v_fma_f32 v215, -v206, v203, v203
	v_mfma_f32_16x16x32_f16 v[164:167], v[64:67], v[128:131], v[116:119]
	s_waitcnt vmcnt(5)
	v_mfma_f32_16x16x32_f16 v[160:163], v[56:59], v[136:139], v[160:163]
	ds_write_b128 v227, v[236:239] offset:4544
	ds_read_b128 v[192:195], v226 offset:4352
	s_waitcnt lgkmcnt(2)
	s_barrier
	ds_read_b128 v[184:187], v209 offset:0
	ds_read_b128 v[188:191], v209 offset:64
	ds_read_b128 v[176:179], v211 offset:0
	ds_read_b128 v[180:183], v211 offset:64
	v_mfma_f32_16x16x32_f16 v[164:167], v[68:71], v[132:135], v[164:167]
	s_waitcnt vmcnt(4)
	v_mfma_f32_16x16x32_f16 v[160:163], v[60:63], v[140:143], v[160:163]
	s_waitcnt lgkmcnt(3)
	v_mfma_f32_16x16x32_f16 v[168:171], v[16:19], v[184:187], v[192:195]
	v_mfma_f32_16x16x32_f16 v[172:175], v[24:27], v[184:187], v[192:195]
	s_waitcnt lgkmcnt(2)
	v_mfma_f32_16x16x32_f16 v[168:171], v[20:23], v[188:191], v[168:171]
	v_mfma_f32_16x16x32_f16 v[172:175], v[28:31], v[188:191], v[172:175]
	s_waitcnt lgkmcnt(1)
	v_mfma_f32_16x16x32_f16 v[168:171], v[32:35], v[176:179], v[168:171]
	v_mfma_f32_16x16x32_f16 v[172:175], v[40:43], v[176:179], v[172:175]
	s_waitcnt lgkmcnt(0)
	v_mfma_f32_16x16x32_f16 v[168:171], v[36:39], v[180:183], v[168:171]
	v_mfma_f32_16x16x32_f16 v[172:175], v[44:47], v[180:183], v[172:175]
	s_nop 7
	v_mov_b32_dpp v168, v172 quad_perm:[0,1,2,3] row_mask:0xf bank_mask:0xa
	v_mov_b32_dpp v169, v173 quad_perm:[0,1,2,3] row_mask:0xf bank_mask:0xa
	v_mov_b32_dpp v170, v174 quad_perm:[0,1,2,3] row_mask:0xf bank_mask:0xa
	v_exp_f32_e32 v200, v168
	v_mov_b32_dpp v171, v175 quad_perm:[0,1,2,3] row_mask:0xf bank_mask:0xa
	v_exp_f32_e32 v201, v169
	v_exp_f32_e32 v202, v170
	v_exp_f32_e32 v203, v171
	v_pk_add_f32 v[200:201], v[200:201], 1.0 op_sel_hi:[1,0]
	v_pk_add_f32 v[202:203], v[202:203], 1.0 op_sel_hi:[1,0]
	v_rcp_f32_e32 v202, v202
	v_rcp_f32_e32 v200, v200
	v_rcp_f32_e32 v201, v201
	v_fmamk_f32 v204, v202, 0xc0b8aa3b, v222
	v_mul_f32_e32 v205, v200, v204
	v_fma_f32 v220, v201, v220, v205
	v_exp_f32_e32 v206, v220
	v_rcp_f32_e32 v203, v203
	v_fma_f32 v206, v206, 0.5, 0.5
	v_rcp_f32_e32 v206, v206
	v_max_f32_e32 v221, v221, v215
	v_fma_mixlo_f16 v208, -v206, v203, v203
	ds_write_b16 v225, v208 offset:576
	v_fma_f32 v215, -v206, v203, v203
	v_mfma_f32_16x16x32_f16 v[232:235], v[80:83], v[128:131], v[120:123]
	v_mfma_f32_16x16x32_f16 v[164:167], v[72:75], v[136:139], v[164:167]
	ds_write_b128 v227, v[160:163] offset:0
	ds_read_b128 v[196:199], v226 offset:5440
	s_waitcnt lgkmcnt(2)
	s_barrier
	ds_read_b128 v[184:187], v210 offset:576
	ds_read_b128 v[188:191], v210 offset:640
	ds_read_b128 v[176:179], v212 offset:576
	ds_read_b128 v[180:183], v212 offset:640
	v_mfma_f32_16x16x32_f16 v[232:235], v[84:87], v[132:135], v[232:235]
	v_mfma_f32_16x16x32_f16 v[164:167], v[76:79], v[140:143], v[164:167]
	s_waitcnt lgkmcnt(3)
	v_mfma_f32_16x16x32_f16 v[168:171], v[16:19], v[184:187], v[196:199]
	v_mfma_f32_16x16x32_f16 v[172:175], v[24:27], v[184:187], v[196:199]
	s_waitcnt lgkmcnt(2)
	v_mfma_f32_16x16x32_f16 v[168:171], v[20:23], v[188:191], v[168:171]
	v_mfma_f32_16x16x32_f16 v[172:175], v[28:31], v[188:191], v[172:175]
	s_waitcnt lgkmcnt(1)
	v_mfma_f32_16x16x32_f16 v[168:171], v[32:35], v[176:179], v[168:171]
	v_mfma_f32_16x16x32_f16 v[172:175], v[40:43], v[176:179], v[172:175]
	s_waitcnt lgkmcnt(0)
	v_mfma_f32_16x16x32_f16 v[168:171], v[36:39], v[180:183], v[168:171]
	v_mfma_f32_16x16x32_f16 v[172:175], v[44:47], v[180:183], v[172:175]
	s_nop 7
	v_mov_b32_dpp v168, v172 quad_perm:[0,1,2,3] row_mask:0xf bank_mask:0xa
	v_mov_b32_dpp v169, v173 quad_perm:[0,1,2,3] row_mask:0xf bank_mask:0xa
	v_mov_b32_dpp v170, v174 quad_perm:[0,1,2,3] row_mask:0xf bank_mask:0xa
	v_exp_f32_e32 v200, v168
	v_mov_b32_dpp v171, v175 quad_perm:[0,1,2,3] row_mask:0xf bank_mask:0xa
	v_exp_f32_e32 v201, v169
	v_exp_f32_e32 v202, v170
	v_exp_f32_e32 v203, v171
	v_pk_add_f32 v[200:201], v[200:201], 1.0 op_sel_hi:[1,0]
	v_pk_add_f32 v[202:203], v[202:203], 1.0 op_sel_hi:[1,0]
	v_rcp_f32_e32 v202, v202
	v_rcp_f32_e32 v200, v200
	v_rcp_f32_e32 v201, v201
	v_fmamk_f32 v204, v202, 0xc0b8aa3b, v222
	v_mul_f32_e32 v205, v200, v204
	v_fma_f32 v220, v201, v220, v205
	v_exp_f32_e32 v206, v220
	v_rcp_f32_e32 v203, v203
	v_fma_f32 v206, v206, 0.5, 0.5
	v_rcp_f32_e32 v206, v206
	v_max_f32_e32 v221, v221, v215
	v_fma_mixlo_f16 v208, -v206, v203, v203
	ds_write_b16 v225, v208 offset:0
	v_fma_f32 v215, -v206, v203, v203
	v_mfma_f32_16x16x32_f16 v[236:239], v[96:99], v[128:131], v[124:127]
	v_mfma_f32_16x16x32_f16 v[232:235], v[88:91], v[136:139], v[232:235]
	global_load_dwordx4 v[128:131], v[228:229], off offset:0
	ds_write_b128 v227, v[164:167] offset:64
	ds_read_b128 v[192:195], v226 offset:6528
	s_waitcnt lgkmcnt(2)
	s_barrier
	ds_read_b128 v[184:187], v209 offset:0
	ds_read_b128 v[188:191], v209 offset:64
	ds_read_b128 v[176:179], v211 offset:0
	ds_read_b128 v[180:183], v211 offset:64
	v_mfma_f32_16x16x32_f16 v[236:239], v[100:103], v[132:135], v[236:239]
	v_mfma_f32_16x16x32_f16 v[232:235], v[92:95], v[140:143], v[232:235]
	global_load_dwordx4 v[132:135], v[228:229], off offset:64
	s_waitcnt lgkmcnt(3)
	v_mfma_f32_16x16x32_f16 v[168:171], v[16:19], v[184:187], v[192:195]
	v_mfma_f32_16x16x32_f16 v[172:175], v[24:27], v[184:187], v[192:195]
	s_waitcnt lgkmcnt(2)
	v_mfma_f32_16x16x32_f16 v[168:171], v[20:23], v[188:191], v[168:171]
	v_mfma_f32_16x16x32_f16 v[172:175], v[28:31], v[188:191], v[172:175]
	s_waitcnt lgkmcnt(1)
	v_mfma_f32_16x16x32_f16 v[168:171], v[32:35], v[176:179], v[168:171]
	v_mfma_f32_16x16x32_f16 v[172:175], v[40:43], v[176:179], v[172:175]
	s_waitcnt lgkmcnt(0)
	v_mfma_f32_16x16x32_f16 v[168:171], v[36:39], v[180:183], v[168:171]
	v_mfma_f32_16x16x32_f16 v[172:175], v[44:47], v[180:183], v[172:175]
	s_nop 7
	v_mov_b32_dpp v168, v172 quad_perm:[0,1,2,3] row_mask:0xf bank_mask:0xa
	v_mov_b32_dpp v169, v173 quad_perm:[0,1,2,3] row_mask:0xf bank_mask:0xa
	v_mov_b32_dpp v170, v174 quad_perm:[0,1,2,3] row_mask:0xf bank_mask:0xa
	v_exp_f32_e32 v200, v168
	v_mov_b32_dpp v171, v175 quad_perm:[0,1,2,3] row_mask:0xf bank_mask:0xa
	v_exp_f32_e32 v201, v169
	v_exp_f32_e32 v202, v170
	v_exp_f32_e32 v203, v171
	v_pk_add_f32 v[200:201], v[200:201], 1.0 op_sel_hi:[1,0]
	v_pk_add_f32 v[202:203], v[202:203], 1.0 op_sel_hi:[1,0]
	v_rcp_f32_e32 v202, v202
	v_rcp_f32_e32 v200, v200
	v_rcp_f32_e32 v201, v201
	v_fmamk_f32 v204, v202, 0xc0b8aa3b, v222
	v_mul_f32_e32 v205, v200, v204
	v_fma_f32 v220, v201, v220, v205
	v_exp_f32_e32 v206, v220
	v_rcp_f32_e32 v203, v203
	v_fma_f32 v206, v206, 0.5, 0.5
	v_rcp_f32_e32 v206, v206
	v_max_f32_e32 v221, v221, v215
	v_fma_mixlo_f16 v208, -v206, v203, v203
	ds_write_b16 v225, v208 offset:576
	v_fma_f32 v215, -v206, v203, v203
	s_waitcnt vmcnt(5)
	v_mfma_f32_16x16x32_f16 v[160:163], v[48:51], v[144:147], v[112:115]
	v_mfma_f32_16x16x32_f16 v[236:239], v[104:107], v[136:139], v[236:239]
	global_load_dwordx4 v[136:139], v[228:229], off offset:128
	ds_write_b128 v227, v[232:235] offset:128
	ds_read_b128 v[196:199], v226 offset:7616
	s_waitcnt lgkmcnt(2)
	s_barrier
	ds_read_b128 v[184:187], v210 offset:576
	ds_read_b128 v[188:191], v210 offset:640
	ds_read_b128 v[176:179], v212 offset:576
	ds_read_b128 v[180:183], v212 offset:640
	s_waitcnt vmcnt(5)
	v_mfma_f32_16x16x32_f16 v[160:163], v[52:55], v[148:151], v[160:163]
	v_mfma_f32_16x16x32_f16 v[236:239], v[108:111], v[140:143], v[236:239]
	global_load_dwordx4 v[140:143], v[228:229], off offset:192
	v_lshl_add_u64 v[228:229], v[228:229], 0, s[20:21]
	s_waitcnt lgkmcnt(3)
	v_mfma_f32_16x16x32_f16 v[168:171], v[16:19], v[184:187], v[196:199]
	v_mfma_f32_16x16x32_f16 v[172:175], v[24:27], v[184:187], v[196:199]
	s_waitcnt lgkmcnt(2)
	v_mfma_f32_16x16x32_f16 v[168:171], v[20:23], v[188:191], v[168:171]
	v_mfma_f32_16x16x32_f16 v[172:175], v[28:31], v[188:191], v[172:175]
	s_waitcnt lgkmcnt(1)
	v_mfma_f32_16x16x32_f16 v[168:171], v[32:35], v[176:179], v[168:171]
	v_mfma_f32_16x16x32_f16 v[172:175], v[40:43], v[176:179], v[172:175]
	s_waitcnt lgkmcnt(0)
	v_mfma_f32_16x16x32_f16 v[168:171], v[36:39], v[180:183], v[168:171]
	v_mfma_f32_16x16x32_f16 v[172:175], v[44:47], v[180:183], v[172:175]
	s_nop 7
	v_mov_b32_dpp v168, v172 quad_perm:[0,1,2,3] row_mask:0xf bank_mask:0xa
	v_mov_b32_dpp v169, v173 quad_perm:[0,1,2,3] row_mask:0xf bank_mask:0xa
	v_mov_b32_dpp v170, v174 quad_perm:[0,1,2,3] row_mask:0xf bank_mask:0xa
	v_exp_f32_e32 v200, v168
	v_mov_b32_dpp v171, v175 quad_perm:[0,1,2,3] row_mask:0xf bank_mask:0xa
	v_exp_f32_e32 v201, v169
	v_exp_f32_e32 v202, v170
	v_exp_f32_e32 v203, v171
	v_pk_add_f32 v[200:201], v[200:201], 1.0 op_sel_hi:[1,0]
	v_pk_add_f32 v[202:203], v[202:203], 1.0 op_sel_hi:[1,0]
	v_rcp_f32_e32 v202, v202
	v_rcp_f32_e32 v200, v200
	v_rcp_f32_e32 v201, v201
	v_fmamk_f32 v204, v202, 0xc0b8aa3b, v222
	v_mul_f32_e32 v205, v200, v204
	v_fma_f32 v220, v201, v220, v205
	v_exp_f32_e32 v206, v220
	v_rcp_f32_e32 v203, v203
	v_fma_f32 v206, v206, 0.5, 0.5
	v_rcp_f32_e32 v206, v206
	v_max_f32_e32 v221, v221, v215
	v_fma_mixlo_f16 v208, -v206, v203, v203
	ds_write_b16 v225, v208 offset:0
	v_fma_f32 v215, -v206, v203, v203
	v_mfma_f32_16x16x32_f16 v[164:167], v[64:67], v[144:147], v[116:119]
	s_waitcnt vmcnt(5)
	v_mfma_f32_16x16x32_f16 v[160:163], v[56:59], v[152:155], v[160:163]
	ds_write_b128 v227, v[236:239] offset:192
	ds_read_b128 v[192:195], v226 offset:0
	s_waitcnt lgkmcnt(2)
	s_barrier
	s_sub_u32 s4, s4, 1
	s_cmp_lg_u32 s4, 0
	s_cbranch_scc1 .Llstm3_loop
	v_max_f32_e32 v221, v221, v215
	global_store_dword v230, v221, s[12:13]
	s_endpgm
